# seam barriers: wave 1 pulls the next 32KB of code into L2 with plain loads while wave 0 runs the barrier (cold instruction fetch hits L2)
# baseline (speedup 1.0000x reference)
.LBB0_57:
	s_cmp_gt_i32 s29, 1
	s_cselect_b64 s[4:5], -1, 0
	s_and_b64 s[0:1], s[62:63], s[4:5]
	s_andn2_b64 vcc, exec, s[0:1]
	s_cbranch_vccnz .LBB0_107
	s_waitcnt vmcnt(0)
	v_cmp_eq_u32_e32 vcc, 0, v0
	s_waitcnt lgkmcnt(0)
	s_barrier
	v_readfirstlane_b32 s100, v0
	s_nop 0
	s_lshr_b32 s100, s100, 6
	s_cmp_lg_u32 s100, 1
	s_cbranch_scc1 .Lipf_skip0
	s_getpc_b64 s[98:99]
	v_lshlrev_b32_e32 v2, 7, v254
	global_load_dword v3, v2, s[98:99]
	s_add_u32 s98, s98, 0x2000
	s_addc_u32 s99, s99, 0
	global_load_dword v3, v2, s[98:99]
	s_add_u32 s98, s98, 0x2000
	s_addc_u32 s99, s99, 0
	global_load_dword v3, v2, s[98:99]
	s_add_u32 s98, s98, 0x2000
	s_addc_u32 s99, s99, 0
	global_load_dword v3, v2, s[98:99]
	s_waitcnt vmcnt(0)
.Lipf_skip0:
	s_and_saveexec_b64 s[0:1], vcc
	s_cbranch_execz .LBB0_106
	v_mov_b32_e32 v2, s88
	s_waitcnt vmcnt(0) expcnt(0) lgkmcnt(0)
	ds_read_b32 v4, v2
	ds_read_b32 v2, v2 offset:4
	s_waitcnt lgkmcnt(1)
	v_cmp_ne_u32_e32 vcc, 0, v4
	s_cbranch_vccnz .LBB0_74
	v_readlane_b32 s6, v255, 0
	v_readlane_b32 s7, v255, 1
	s_load_dwordx2 s[18:19], s[6:7], 0x4
	s_add_u32 s6, s30, 0x1000
	s_addc_u32 s7, s31, 0
	s_add_u32 s8, s30, 0x1100
	s_addc_u32 s9, s31, 0
	s_waitcnt lgkmcnt(0)
	s_mul_i32 s3, s18, s33
	s_add_u32 s18, s30, 0x1200
	s_mul_i32 s3, s3, s19
	s_addc_u32 s19, s31, 0
	s_add_u32 s22, s30, 0x1300
	s_addc_u32 s23, s31, 0
	s_mov_b32 s34, 1
	v_mov_b32_e32 v18, 0
	s_branch .LBB0_62

.LBB0_115:
	s_cmp_gt_i32 s29, 2
	s_cselect_b64 s[6:7], -1, 0
	s_and_b64 s[0:1], s[0:1], s[6:7]
	s_andn2_b64 vcc, exec, s[0:1]
	s_cbranch_vccnz .LBB0_165
	s_waitcnt vmcnt(0)
	v_cmp_eq_u32_e32 vcc, 0, v0
	s_waitcnt lgkmcnt(0)
	s_barrier
	v_readfirstlane_b32 s100, v0
	s_nop 0
	s_lshr_b32 s100, s100, 6
	s_cmp_lg_u32 s100, 1
	s_cbranch_scc1 .Lipf_skip1
	s_getpc_b64 s[98:99]
	v_lshlrev_b32_e32 v2, 7, v254
	global_load_dword v3, v2, s[98:99]
	s_add_u32 s98, s98, 0x2000
	s_addc_u32 s99, s99, 0
	global_load_dword v3, v2, s[98:99]
	s_add_u32 s98, s98, 0x2000
	s_addc_u32 s99, s99, 0
	global_load_dword v3, v2, s[98:99]
	s_add_u32 s98, s98, 0x2000
	s_addc_u32 s99, s99, 0
	global_load_dword v3, v2, s[98:99]
	s_waitcnt vmcnt(0)
.Lipf_skip1:
	s_and_saveexec_b64 s[0:1], vcc
	s_cbranch_execz .LBB0_164
	v_mov_b32_e32 v2, s88
	s_waitcnt vmcnt(0) expcnt(0) lgkmcnt(0)
	ds_read_b32 v4, v2
	ds_read_b32 v2, v2 offset:4
	s_waitcnt lgkmcnt(1)
	v_cmp_ne_u32_e32 vcc, 0, v4
	s_cbranch_vccnz .LBB0_132
	v_readlane_b32 s4, v255, 0
	v_readlane_b32 s5, v255, 1
	s_load_dwordx2 s[18:19], s[4:5], 0x4
	s_add_u32 s4, s30, 0x1000
	s_addc_u32 s5, s31, 0
	s_add_u32 s8, s30, 0x1100
	s_addc_u32 s9, s31, 0
	s_waitcnt lgkmcnt(0)
	s_mul_i32 s3, s18, s33
	s_add_u32 s18, s30, 0x1200
	s_mul_i32 s3, s3, s19
	s_addc_u32 s19, s31, 0
	s_add_u32 s22, s30, 0x1300
	s_addc_u32 s23, s31, 0
	s_mov_b32 s34, 1
	v_mov_b32_e32 v18, 0
	s_branch .LBB0_120

.LBB0_216:
	s_cmp_gt_i32 s29, 3
	s_cselect_b64 s[0:1], -1, 0
	s_and_b64 s[4:5], s[4:5], s[0:1]
	s_andn2_b64 vcc, exec, s[4:5]
	s_cbranch_vccnz .LBB0_266
	s_waitcnt vmcnt(0)
	v_cmp_eq_u32_e32 vcc, 0, v0
	s_waitcnt vmcnt(0) lgkmcnt(0)
	s_barrier
	v_readfirstlane_b32 s100, v0
	s_nop 0
	s_lshr_b32 s100, s100, 6
	s_cmp_lg_u32 s100, 1
	s_cbranch_scc1 .Lipf_skip2
	s_getpc_b64 s[98:99]
	v_lshlrev_b32_e32 v2, 7, v254
	global_load_dword v3, v2, s[98:99]
	s_add_u32 s98, s98, 0x2000
	s_addc_u32 s99, s99, 0
	global_load_dword v3, v2, s[98:99]
	s_add_u32 s98, s98, 0x2000
	s_addc_u32 s99, s99, 0
	global_load_dword v3, v2, s[98:99]
	s_add_u32 s98, s98, 0x2000
	s_addc_u32 s99, s99, 0
	global_load_dword v3, v2, s[98:99]
	s_waitcnt vmcnt(0)
.Lipf_skip2:
	s_and_saveexec_b64 s[4:5], vcc
	s_cbranch_execz .LBB0_265
	v_mov_b32_e32 v2, s88
	s_waitcnt vmcnt(0) expcnt(0) lgkmcnt(0)
	ds_read_b32 v4, v2
	ds_read_b32 v2, v2 offset:4
	s_waitcnt lgkmcnt(1)
	v_cmp_ne_u32_e32 vcc, 0, v4
	s_cbranch_vccnz .LBB0_233
	v_readlane_b32 s6, v255, 0
	v_readlane_b32 s7, v255, 1
	s_load_dwordx2 s[12:13], s[6:7], 0x4
	s_add_u32 s6, s30, 0x1000
	s_addc_u32 s7, s31, 0
	s_add_u32 s8, s30, 0x1100
	s_addc_u32 s9, s31, 0
	s_waitcnt lgkmcnt(0)
	s_mul_i32 s3, s12, s33
	s_add_u32 s12, s30, 0x1200
	s_mul_i32 s3, s3, s13
	s_addc_u32 s13, s31, 0
	s_add_u32 s14, s30, 0x1300
	s_addc_u32 s15, s31, 0
	s_mov_b32 s34, 1
	v_mov_b32_e32 v18, 0
	s_branch .LBB0_221

.LBB0_271:
	s_cmp_gt_i32 s29, 4
	s_cselect_b64 s[0:1], -1, 0
	s_and_b64 s[4:5], s[4:5], s[0:1]
	s_andn2_b64 vcc, exec, s[4:5]
	s_cbranch_vccnz .LBB0_321
	s_waitcnt vmcnt(0)
	v_cmp_eq_u32_e32 vcc, 0, v0
	s_waitcnt vmcnt(0) lgkmcnt(0)
	s_barrier
	v_readfirstlane_b32 s100, v0
	s_nop 0
	s_lshr_b32 s100, s100, 6
	s_cmp_lg_u32 s100, 1
	s_cbranch_scc1 .Lipf_skip3
	s_getpc_b64 s[98:99]
	v_lshlrev_b32_e32 v2, 7, v254
	global_load_dword v3, v2, s[98:99]
	s_add_u32 s98, s98, 0x2000
	s_addc_u32 s99, s99, 0
	global_load_dword v3, v2, s[98:99]
	s_add_u32 s98, s98, 0x2000
	s_addc_u32 s99, s99, 0
	global_load_dword v3, v2, s[98:99]
	s_add_u32 s98, s98, 0x2000
	s_addc_u32 s99, s99, 0
	global_load_dword v3, v2, s[98:99]
	s_waitcnt vmcnt(0)
.Lipf_skip3:
	s_and_saveexec_b64 s[4:5], vcc
	s_cbranch_execz .LBB0_320
	v_mov_b32_e32 v2, s88
	s_waitcnt vmcnt(0) expcnt(0) lgkmcnt(0)
	ds_read_b32 v4, v2
	ds_read_b32 v2, v2 offset:4
	s_waitcnt lgkmcnt(1)
	v_cmp_ne_u32_e32 vcc, 0, v4
	s_cbranch_vccnz .LBB0_288
	v_readlane_b32 s8, v255, 0
	v_readlane_b32 s9, v255, 1
	s_load_dwordx2 s[14:15], s[8:9], 0x4
	s_add_u32 s8, s30, 0x1000
	s_addc_u32 s9, s31, 0
	s_add_u32 s12, s30, 0x1100
	s_addc_u32 s13, s31, 0
	s_waitcnt lgkmcnt(0)
	s_mul_i32 s3, s14, s33
	s_add_u32 s14, s30, 0x1200
	s_mul_i32 s3, s3, s15
	s_addc_u32 s15, s31, 0
	s_add_u32 s18, s30, 0x1300
	s_addc_u32 s19, s31, 0
	s_mov_b32 s34, 1
	v_mov_b32_e32 v18, 0
	s_branch .LBB0_276

.LBB0_337:
	s_cmp_gt_i32 s29, 5
	s_cselect_b64 s[0:1], -1, 0
	s_and_b64 s[4:5], s[8:9], s[0:1]
	s_andn2_b64 vcc, exec, s[4:5]
	s_cbranch_vccnz .LBB0_387
	s_waitcnt vmcnt(0)
	v_cmp_eq_u32_e32 vcc, 0, v0
	s_waitcnt vmcnt(0) lgkmcnt(0)
	s_barrier
	v_readfirstlane_b32 s100, v0
	s_nop 0
	s_lshr_b32 s100, s100, 6
	s_cmp_lg_u32 s100, 1
	s_cbranch_scc1 .Lipf_skip4
	s_getpc_b64 s[98:99]
	v_lshlrev_b32_e32 v2, 7, v254
	global_load_dword v3, v2, s[98:99]
	s_add_u32 s98, s98, 0x2000
	s_addc_u32 s99, s99, 0
	global_load_dword v3, v2, s[98:99]
	s_add_u32 s98, s98, 0x2000
	s_addc_u32 s99, s99, 0
	global_load_dword v3, v2, s[98:99]
	s_add_u32 s98, s98, 0x2000
	s_addc_u32 s99, s99, 0
	global_load_dword v3, v2, s[98:99]
	s_waitcnt vmcnt(0)

.LBB0_401:
	s_cmp_gt_i32 s29, 6
	s_cselect_b64 s[0:1], -1, 0
	s_and_b64 s[4:5], s[12:13], s[0:1]
	s_andn2_b64 vcc, exec, s[4:5]
	s_cbranch_vccnz .LBB0_451
	s_waitcnt vmcnt(0)
	v_cmp_eq_u32_e32 vcc, 0, v0
	s_waitcnt vmcnt(0)
	s_barrier
	v_readfirstlane_b32 s100, v0
	s_nop 0
	s_lshr_b32 s100, s100, 6
	s_cmp_lg_u32 s100, 1
	s_cbranch_scc1 .Lipf_skip5
	s_getpc_b64 s[98:99]
	v_lshlrev_b32_e32 v2, 7, v254
	global_load_dword v3, v2, s[98:99]
	s_add_u32 s98, s98, 0x2000
	s_addc_u32 s99, s99, 0
	global_load_dword v3, v2, s[98:99]
	s_add_u32 s98, s98, 0x2000
	s_addc_u32 s99, s99, 0
	global_load_dword v3, v2, s[98:99]
	s_add_u32 s98, s98, 0x2000
	s_addc_u32 s99, s99, 0
	global_load_dword v3, v2, s[98:99]
	s_waitcnt vmcnt(0)
.Lipf_skip5:
	s_and_saveexec_b64 s[4:5], vcc
	s_cbranch_execz .LBB0_450
	v_mov_b32_e32 v1, s88
	s_waitcnt vmcnt(0) expcnt(0) lgkmcnt(0)
	ds_read_b32 v3, v1
	ds_read_b32 v1, v1 offset:4
	s_waitcnt lgkmcnt(1)
	v_cmp_ne_u32_e32 vcc, 0, v3
	s_cbranch_vccnz .LBB0_418
	v_readlane_b32 s6, v255, 0
	v_readlane_b32 s7, v255, 1
	s_load_dwordx2 s[12:13], s[6:7], 0x4
	s_add_u32 s6, s30, 0x1000
	s_addc_u32 s7, s31, 0
	s_add_u32 s8, s30, 0x1100
	s_addc_u32 s9, s31, 0
	s_waitcnt lgkmcnt(0)
	s_mul_i32 s3, s12, s33
	s_add_u32 s12, s30, 0x1200
	s_mul_i32 s3, s3, s13
	s_addc_u32 s13, s31, 0
	s_add_u32 s14, s30, 0x1300
	s_addc_u32 s15, s31, 0
	s_mov_b32 s34, 1
	v_mov_b32_e32 v17, 0
	s_branch .LBB0_406

.LBB0_482:
	s_cmp_gt_i32 s29, 7
	s_cselect_b64 s[0:1], -1, 0
	s_and_b64 s[4:5], s[6:7], s[0:1]
	s_andn2_b64 vcc, exec, s[4:5]
	s_cbranch_vccnz .LBB0_532
	s_waitcnt vmcnt(0)
	v_cmp_eq_u32_e32 vcc, 0, v0
	s_waitcnt vmcnt(0)
	s_barrier
	v_readfirstlane_b32 s100, v0
	s_nop 0
	s_lshr_b32 s100, s100, 6
	s_cmp_lg_u32 s100, 1
	s_cbranch_scc1 .Lipf_skip6
	s_getpc_b64 s[98:99]
	v_lshlrev_b32_e32 v2, 7, v254
	global_load_dword v3, v2, s[98:99]
	s_add_u32 s98, s98, 0x2000
	s_addc_u32 s99, s99, 0
	global_load_dword v3, v2, s[98:99]
	s_add_u32 s98, s98, 0x2000
	s_addc_u32 s99, s99, 0
	global_load_dword v3, v2, s[98:99]
	s_add_u32 s98, s98, 0x2000
	s_addc_u32 s99, s99, 0
	global_load_dword v3, v2, s[98:99]
	s_waitcnt vmcnt(0)

.LBB0_557:
	s_cmp_gt_i32 s29, 8
	s_cselect_b64 s[0:1], -1, 0
	s_and_b64 s[4:5], s[4:5], s[0:1]
	s_andn2_b64 vcc, exec, s[4:5]
	s_cbranch_vccnz .LBB0_607
	s_waitcnt vmcnt(0)
	v_cmp_eq_u32_e32 vcc, 0, v0
	s_waitcnt vmcnt(0)
	s_barrier
	v_readfirstlane_b32 s100, v0
	s_nop 0
	s_lshr_b32 s100, s100, 6
	s_cmp_lg_u32 s100, 1
	s_cbranch_scc1 .Lipf_skip7
	s_getpc_b64 s[98:99]
	v_lshlrev_b32_e32 v2, 7, v254
	global_load_dword v3, v2, s[98:99]
	s_add_u32 s98, s98, 0x2000
	s_addc_u32 s99, s99, 0
	global_load_dword v3, v2, s[98:99]
	s_add_u32 s98, s98, 0x2000
	s_addc_u32 s99, s99, 0
	global_load_dword v3, v2, s[98:99]
	s_add_u32 s98, s98, 0x2000
	s_addc_u32 s99, s99, 0
	global_load_dword v3, v2, s[98:99]
	s_waitcnt vmcnt(0)

.LBB0_623:
	s_cmp_gt_i32 s29, 9
	s_cselect_b64 s[0:1], -1, 0
	s_and_b64 s[2:3], s[12:13], s[0:1]
	s_andn2_b64 vcc, exec, s[2:3]
	s_cbranch_vccnz .LBB0_673
	s_waitcnt vmcnt(0)
	v_cmp_eq_u32_e32 vcc, 0, v0
	s_waitcnt vmcnt(0)
	s_barrier
	v_readfirstlane_b32 s100, v0
	s_nop 0
	s_lshr_b32 s100, s100, 6
	s_cmp_lg_u32 s100, 1
	s_cbranch_scc1 .Lipf_skip8
	s_getpc_b64 s[98:99]
	v_lshlrev_b32_e32 v2, 7, v254
	global_load_dword v3, v2, s[98:99]
	s_add_u32 s98, s98, 0x2000
	s_addc_u32 s99, s99, 0
	global_load_dword v3, v2, s[98:99]
	s_add_u32 s98, s98, 0x2000
	s_addc_u32 s99, s99, 0
	global_load_dword v3, v2, s[98:99]
	s_add_u32 s98, s98, 0x2000
	s_addc_u32 s99, s99, 0
	global_load_dword v3, v2, s[98:99]
	s_waitcnt vmcnt(0)
.Lipf_skip8:
	s_and_saveexec_b64 s[2:3], vcc
	s_cbranch_execz .LBB0_672
	v_mov_b32_e32 v1, s88
	s_waitcnt vmcnt(0) expcnt(0) lgkmcnt(0)
	ds_read_b32 v3, v1
	ds_read_b32 v1, v1 offset:4
	s_waitcnt lgkmcnt(1)
	v_cmp_ne_u32_e32 vcc, 0, v3
	s_cbranch_vccnz .LBB0_640
	v_readlane_b32 s4, v255, 0
	v_readlane_b32 s5, v255, 1
	s_load_dwordx2 s[8:9], s[4:5], 0x4
	s_add_u32 s4, s30, 0x1000
	s_addc_u32 s5, s31, 0
	s_add_u32 s6, s30, 0x1100
	s_addc_u32 s7, s31, 0
	s_waitcnt lgkmcnt(0)
	s_mul_i32 s20, s8, s33
	s_add_u32 s8, s30, 0x1200
	s_mul_i32 s20, s20, s9
	s_addc_u32 s9, s31, 0
	s_add_u32 s12, s30, 0x1300
	s_addc_u32 s13, s31, 0
	s_mov_b32 s21, 1
	v_mov_b32_e32 v17, 0
	s_branch .LBB0_628

.LBB0_741:
	s_cmp_gt_i32 s29, 10
	s_cselect_b64 s[0:1], -1, 0
	s_and_b64 s[2:3], s[6:7], s[0:1]
	s_andn2_b64 vcc, exec, s[2:3]
	s_cbranch_vccnz .LBB0_806
	s_waitcnt vmcnt(0)
	v_cmp_eq_u32_e32 vcc, 0, v0
	s_waitcnt vmcnt(0) lgkmcnt(0)
	s_barrier
	v_readfirstlane_b32 s100, v0
	s_nop 0
	s_lshr_b32 s100, s100, 6
	s_cmp_lg_u32 s100, 1
	s_cbranch_scc1 .Lipf_skip9
	s_getpc_b64 s[98:99]
	v_lshlrev_b32_e32 v2, 7, v254
	global_load_dword v3, v2, s[98:99]
	s_add_u32 s98, s98, 0x2000
	s_addc_u32 s99, s99, 0
	global_load_dword v3, v2, s[98:99]
	s_waitcnt vmcnt(0)

.LBB0_876:
	s_waitcnt vmcnt(0)
	s_waitcnt vmcnt(0) lgkmcnt(0)
	s_barrier
	s_lshr_b32 s100, s87, 6
	s_cmp_lg_u32 s100, 1
	s_cbranch_scc1 .Lipf_skip10
	s_getpc_b64 s[98:99]
	v_mul_u32_u24_e32 v2, 96, v254
	global_load_dword v3, v2, s[98:99]
	s_waitcnt vmcnt(0)
.Lipf_skip10:
	s_and_saveexec_b64 s[2:3], s[4:5]
	s_cbranch_execz .LBB0_939
	v_mov_b32_e32 v0, s88
	s_waitcnt vmcnt(0) expcnt(0) lgkmcnt(0)
	ds_read_b32 v2, v0
	ds_read_b32 v0, v0 offset:4
	s_waitcnt lgkmcnt(1)
	v_cmp_ne_u32_e32 vcc, 0, v2
	s_cbranch_vccnz .LBB0_892
	v_readlane_b32 s4, v255, 0
	v_readlane_b32 s5, v255, 1
	s_load_dwordx2 s[8:9], s[4:5], 0x4
	s_add_u32 s4, s30, 0x1000
	s_addc_u32 s5, s31, 0
	s_add_u32 s6, s30, 0x1100
	s_addc_u32 s7, s31, 0
	s_waitcnt lgkmcnt(0)
	s_mul_i32 s20, s8, s33
	s_add_u32 s8, s30, 0x1200
	s_mul_i32 s20, s20, s9
	s_addc_u32 s9, s31, 0
	s_add_u32 s12, s30, 0x1300
	s_addc_u32 s13, s31, 0
	s_mov_b32 s21, 1
	v_mov_b32_e32 v16, 0
	s_branch .LBB0_880
